# speedup vs baseline: 1.0011x; 1.0011x over previous
.LBB0_46:
	s_or_b64 exec, exec, s[4:5]
	v_lshlrev_b32_e32 v2, 5, v44
	s_waitcnt lgkmcnt(0)
	s_barrier
	ds_read_b128 v[14:17], v2 offset:20480
	ds_read_b128 v[2:5], v2 offset:20496
	v_mov_b32_e32 v41, 0
	v_lshlrev_b32_e32 v40, 4, v1
	s_waitcnt lgkmcnt(1)
	v_cmp_gt_i32_e64 s[16:17], 0, v14
	v_max_i32_e32 v42, 0, v14
	v_lshl_add_u32 v42, v42, 10, v40
	global_load_dwordx4 v[48:51], v42, s[24:25] nt
	v_cmp_gt_i32_e64 s[14:15], 0, v15
	v_max_i32_e32 v43, 0, v15
	v_lshl_add_u32 v43, v43, 10, v40
	global_load_dwordx4 v[34:37], v43, s[24:25] nt
	v_cmp_gt_i32_e64 s[12:13], 0, v16
	v_max_i32_e32 v42, 0, v16
	v_lshl_add_u32 v42, v42, 10, v40
	global_load_dwordx4 v[30:33], v42, s[24:25] nt
	v_cmp_gt_i32_e64 s[10:11], 0, v17
	v_max_i32_e32 v43, 0, v17
	v_lshl_add_u32 v43, v43, 10, v40
	global_load_dwordx4 v[26:29], v43, s[24:25] nt
	s_waitcnt lgkmcnt(0)
	v_cmp_gt_i32_e64 s[8:9], 0, v2
	v_max_i32_e32 v42, 0, v2
	v_lshl_add_u32 v42, v42, 10, v40
	global_load_dwordx4 v[22:25], v42, s[24:25] nt
	v_cmp_gt_i32_e64 s[6:7], 0, v3
	v_max_i32_e32 v43, 0, v3
	v_lshl_add_u32 v43, v43, 10, v40
	global_load_dwordx4 v[18:21], v43, s[24:25] nt
	v_cmp_gt_i32_e64 s[4:5], 0, v4
	v_max_i32_e32 v42, 0, v4
	v_lshl_add_u32 v42, v42, 10, v40
	global_load_dwordx4 v[10:13], v42, s[24:25] nt
	v_cmp_gt_i32_e64 s[2:3], 0, v5
	v_max_i32_e32 v43, 0, v5
	v_lshl_add_u32 v43, v43, 10, v40
	global_load_dwordx4 v[6:9], v43, s[24:25] nt
	v_lshlrev_b32_e32 v1, 8, v0
	v_lshlrev_b32_e32 v0, 3, v0
	s_movk_i32 s19, 0x3c00
	v_and_b32_e32 v0, 8, v0
	v_and_or_b32 v46, v1, s19, v0
	s_mul_i32 s18, s20, 0x4080
	s_mul_hi_u32 s24, s20, 0x4080
	s_add_u32 s18, s22, s18
	v_lshlrev_b32_e32 v39, 3, v44
	v_and_b32_e32 v41, 32, v38
	s_addc_u32 s19, s23, s24
	s_add_u32 s22, s18, 0x4000
	s_addc_u32 s23, s19, 0
	v_add_u32_e32 v60, v39, v41
	v_lshl_add_u32 v60, v60, 4, v46
	v_lshrrev_b32_e32 v67, 1, v40
	v_and_b32_e32 v67, 0x70, v67
	v_or_b32_e32 v67, v60, v67
	v_mov_b32_e32 v66, 0xff800000
	s_waitcnt vmcnt(7)
	v_cndmask_b32_e64 v48, v48, 0, s[16:17]
	v_cndmask_b32_e64 v49, v49, 0, s[16:17]
	v_cndmask_b32_e64 v50, v50, 0, s[16:17]
	v_cndmask_b32_e64 v51, v51, 0, s[16:17]
	v_pk_mul_f32 v[62:63], v[48:49], v[48:49]
	v_pk_mul_f32 v[64:65], v[50:51], v[50:51]
	v_add_f32_e32 v52, v62, v63
	v_add_f32_e32 v52, v52, v64
	v_add_f32_e32 v52, v52, v65
	v_cvt_pk_f16_f32 v62, v48, v49
	v_cvt_pk_f16_f32 v63, v50, v51
	ds_write_b64 v67, v[62:63]
	s_waitcnt vmcnt(6)
	v_cndmask_b32_e64 v34, v34, 0, s[14:15]
	v_cndmask_b32_e64 v35, v35, 0, s[14:15]
	v_cndmask_b32_e64 v36, v36, 0, s[14:15]
	v_cndmask_b32_e64 v37, v37, 0, s[14:15]
	v_pk_mul_f32 v[62:63], v[34:35], v[34:35]
	v_pk_mul_f32 v[64:65], v[36:37], v[36:37]
	v_add_f32_e32 v53, v62, v63
	v_add_f32_e32 v53, v53, v64
	v_add_f32_e32 v53, v53, v65
	v_cvt_pk_f16_f32 v62, v34, v35
	v_cvt_pk_f16_f32 v63, v36, v37
	v_xor_b32_e32 v68, 0x10, v67
	ds_write_b64 v68, v[62:63]
	s_waitcnt vmcnt(5)
	v_cndmask_b32_e64 v30, v30, 0, s[12:13]
	v_cndmask_b32_e64 v31, v31, 0, s[12:13]
	v_cndmask_b32_e64 v32, v32, 0, s[12:13]
	v_cndmask_b32_e64 v33, v33, 0, s[12:13]
	v_pk_mul_f32 v[62:63], v[30:31], v[30:31]
	v_pk_mul_f32 v[64:65], v[32:33], v[32:33]
	v_add_f32_e32 v54, v62, v63
	v_add_f32_e32 v54, v54, v64
	v_add_f32_e32 v54, v54, v65
	v_cvt_pk_f16_f32 v62, v30, v31
	v_cvt_pk_f16_f32 v63, v32, v33
	v_xor_b32_e32 v68, 0x20, v67
	ds_write_b64 v68, v[62:63]
	s_waitcnt vmcnt(4)
	v_cndmask_b32_e64 v26, v26, 0, s[10:11]
	v_cndmask_b32_e64 v27, v27, 0, s[10:11]
	v_cndmask_b32_e64 v28, v28, 0, s[10:11]
	v_cndmask_b32_e64 v29, v29, 0, s[10:11]
	v_pk_mul_f32 v[62:63], v[26:27], v[26:27]
	v_pk_mul_f32 v[64:65], v[28:29], v[28:29]
	v_add_f32_e32 v55, v62, v63
	v_add_f32_e32 v55, v55, v64
	v_add_f32_e32 v55, v55, v65
	v_cvt_pk_f16_f32 v62, v26, v27
	v_cvt_pk_f16_f32 v63, v28, v29
	v_xor_b32_e32 v68, 0x30, v67
	ds_write_b64 v68, v[62:63]
	s_waitcnt vmcnt(3)
	v_cndmask_b32_e64 v22, v22, 0, s[8:9]
	v_cndmask_b32_e64 v23, v23, 0, s[8:9]
	v_cndmask_b32_e64 v24, v24, 0, s[8:9]
	v_cndmask_b32_e64 v25, v25, 0, s[8:9]
	v_pk_mul_f32 v[62:63], v[22:23], v[22:23]
	v_pk_mul_f32 v[64:65], v[24:25], v[24:25]
	v_add_f32_e32 v56, v62, v63
	v_add_f32_e32 v56, v56, v64
	v_add_f32_e32 v56, v56, v65
	v_cvt_pk_f16_f32 v62, v22, v23
	v_cvt_pk_f16_f32 v63, v24, v25
	v_xor_b32_e32 v68, 0x40, v67
	ds_write_b64 v68, v[62:63]
	s_waitcnt vmcnt(2)
	v_cndmask_b32_e64 v18, v18, 0, s[6:7]
	v_cndmask_b32_e64 v19, v19, 0, s[6:7]
	v_cndmask_b32_e64 v20, v20, 0, s[6:7]
	v_cndmask_b32_e64 v21, v21, 0, s[6:7]
	v_pk_mul_f32 v[62:63], v[18:19], v[18:19]
	v_pk_mul_f32 v[64:65], v[20:21], v[20:21]
	v_add_f32_e32 v57, v62, v63
	v_add_f32_e32 v57, v57, v64
	v_add_f32_e32 v57, v57, v65
	v_cvt_pk_f16_f32 v62, v18, v19
	v_cvt_pk_f16_f32 v63, v20, v21
	v_xor_b32_e32 v68, 0x50, v67
	ds_write_b64 v68, v[62:63]
	s_waitcnt vmcnt(1)
	v_cndmask_b32_e64 v10, v10, 0, s[4:5]
	v_cndmask_b32_e64 v11, v11, 0, s[4:5]
	v_cndmask_b32_e64 v12, v12, 0, s[4:5]
	v_cndmask_b32_e64 v13, v13, 0, s[4:5]
	v_pk_mul_f32 v[62:63], v[10:11], v[10:11]
	v_pk_mul_f32 v[64:65], v[12:13], v[12:13]
	v_add_f32_e32 v58, v62, v63
	v_add_f32_e32 v58, v58, v64
	v_add_f32_e32 v58, v58, v65
	v_cvt_pk_f16_f32 v62, v10, v11
	v_cvt_pk_f16_f32 v63, v12, v13
	v_xor_b32_e32 v68, 0x60, v67
	ds_write_b64 v68, v[62:63]
	s_waitcnt vmcnt(0)
	v_cndmask_b32_e64 v6, v6, 0, s[2:3]
	v_cndmask_b32_e64 v7, v7, 0, s[2:3]
	v_cndmask_b32_e64 v8, v8, 0, s[2:3]
	v_cndmask_b32_e64 v9, v9, 0, s[2:3]
	v_pk_mul_f32 v[62:63], v[6:7], v[6:7]
	v_pk_mul_f32 v[64:65], v[8:9], v[8:9]
	v_add_f32_e32 v59, v62, v63
	v_add_f32_e32 v59, v59, v64
	v_add_f32_e32 v59, v59, v65
	v_cvt_pk_f16_f32 v62, v6, v7
	v_cvt_pk_f16_f32 v63, v8, v9
	v_xor_b32_e32 v68, 0x70, v67
	ds_write_b64 v68, v[62:63]
	v_add_f32_dpp v52, v52, v52 quad_perm:[1,0,3,2] row_mask:0xf bank_mask:0xf bound_ctrl:1
	v_add_f32_dpp v53, v53, v53 quad_perm:[1,0,3,2] row_mask:0xf bank_mask:0xf bound_ctrl:1
	v_add_f32_dpp v54, v54, v54 quad_perm:[1,0,3,2] row_mask:0xf bank_mask:0xf bound_ctrl:1
	v_add_f32_dpp v55, v55, v55 quad_perm:[1,0,3,2] row_mask:0xf bank_mask:0xf bound_ctrl:1
	v_add_f32_dpp v56, v56, v56 quad_perm:[1,0,3,2] row_mask:0xf bank_mask:0xf bound_ctrl:1
	v_add_f32_dpp v57, v57, v57 quad_perm:[1,0,3,2] row_mask:0xf bank_mask:0xf bound_ctrl:1
	v_add_f32_dpp v58, v58, v58 quad_perm:[1,0,3,2] row_mask:0xf bank_mask:0xf bound_ctrl:1
	v_add_f32_dpp v59, v59, v59 quad_perm:[1,0,3,2] row_mask:0xf bank_mask:0xf bound_ctrl:1
	v_add_f32_dpp v52, v52, v52 quad_perm:[2,3,0,1] row_mask:0xf bank_mask:0xf bound_ctrl:1
	v_add_f32_dpp v53, v53, v53 quad_perm:[2,3,0,1] row_mask:0xf bank_mask:0xf bound_ctrl:1
	v_add_f32_dpp v54, v54, v54 quad_perm:[2,3,0,1] row_mask:0xf bank_mask:0xf bound_ctrl:1
	v_add_f32_dpp v55, v55, v55 quad_perm:[2,3,0,1] row_mask:0xf bank_mask:0xf bound_ctrl:1
	v_add_f32_dpp v56, v56, v56 quad_perm:[2,3,0,1] row_mask:0xf bank_mask:0xf bound_ctrl:1
	v_add_f32_dpp v57, v57, v57 quad_perm:[2,3,0,1] row_mask:0xf bank_mask:0xf bound_ctrl:1
	v_add_f32_dpp v58, v58, v58 quad_perm:[2,3,0,1] row_mask:0xf bank_mask:0xf bound_ctrl:1
	v_add_f32_dpp v59, v59, v59 quad_perm:[2,3,0,1] row_mask:0xf bank_mask:0xf bound_ctrl:1
	v_add_f32_dpp v52, v52, v52 row_half_mirror row_mask:0xf bank_mask:0xf bound_ctrl:1
	v_add_f32_dpp v53, v53, v53 row_half_mirror row_mask:0xf bank_mask:0xf bound_ctrl:1
	v_add_f32_dpp v54, v54, v54 row_half_mirror row_mask:0xf bank_mask:0xf bound_ctrl:1
	v_add_f32_dpp v55, v55, v55 row_half_mirror row_mask:0xf bank_mask:0xf bound_ctrl:1
	v_add_f32_dpp v56, v56, v56 row_half_mirror row_mask:0xf bank_mask:0xf bound_ctrl:1
	v_add_f32_dpp v57, v57, v57 row_half_mirror row_mask:0xf bank_mask:0xf bound_ctrl:1
	v_add_f32_dpp v58, v58, v58 row_half_mirror row_mask:0xf bank_mask:0xf bound_ctrl:1
	v_add_f32_dpp v59, v59, v59 row_half_mirror row_mask:0xf bank_mask:0xf bound_ctrl:1
	v_add_f32_dpp v52, v52, v52 row_mirror row_mask:0xf bank_mask:0xf bound_ctrl:1
	v_add_f32_dpp v53, v53, v53 row_mirror row_mask:0xf bank_mask:0xf bound_ctrl:1
	v_add_f32_dpp v54, v54, v54 row_mirror row_mask:0xf bank_mask:0xf bound_ctrl:1
	v_add_f32_dpp v55, v55, v55 row_mirror row_mask:0xf bank_mask:0xf bound_ctrl:1
	v_add_f32_dpp v56, v56, v56 row_mirror row_mask:0xf bank_mask:0xf bound_ctrl:1
	v_add_f32_dpp v57, v57, v57 row_mirror row_mask:0xf bank_mask:0xf bound_ctrl:1
	v_add_f32_dpp v58, v58, v58 row_mirror row_mask:0xf bank_mask:0xf bound_ctrl:1
	v_add_f32_dpp v59, v59, v59 row_mirror row_mask:0xf bank_mask:0xf bound_ctrl:1
	v_add_f32_dpp v52, v52, v52 row_bcast:15 row_mask:0xa bank_mask:0xf
	v_add_f32_dpp v53, v53, v53 row_bcast:15 row_mask:0xa bank_mask:0xf
	v_add_f32_dpp v54, v54, v54 row_bcast:15 row_mask:0xa bank_mask:0xf
	v_add_f32_dpp v55, v55, v55 row_bcast:15 row_mask:0xa bank_mask:0xf
	v_add_f32_dpp v56, v56, v56 row_bcast:15 row_mask:0xa bank_mask:0xf
	v_add_f32_dpp v57, v57, v57 row_bcast:15 row_mask:0xa bank_mask:0xf
	v_add_f32_dpp v58, v58, v58 row_bcast:15 row_mask:0xa bank_mask:0xf
	v_add_f32_dpp v59, v59, v59 row_bcast:15 row_mask:0xa bank_mask:0xf
	v_add_f32_dpp v52, v52, v52 row_bcast:31 row_mask:0xc bank_mask:0xf
	v_add_f32_dpp v53, v53, v53 row_bcast:31 row_mask:0xc bank_mask:0xf
	v_add_f32_dpp v54, v54, v54 row_bcast:31 row_mask:0xc bank_mask:0xf
	v_add_f32_dpp v55, v55, v55 row_bcast:31 row_mask:0xc bank_mask:0xf
	v_add_f32_dpp v56, v56, v56 row_bcast:31 row_mask:0xc bank_mask:0xf
	v_add_f32_dpp v57, v57, v57 row_bcast:31 row_mask:0xc bank_mask:0xf
	v_add_f32_dpp v58, v58, v58 row_bcast:31 row_mask:0xc bank_mask:0xf
	v_add_f32_dpp v59, v59, v59 row_bcast:31 row_mask:0xc bank_mask:0xf
	v_pk_add_f32 v[0:1], v[48:49], 0 op_sel_hi:[1,0]
	v_pk_add_f32 v[2:3], v[50:51], 0 op_sel_hi:[1,0]
	v_pk_add_f32 v[0:1], v[0:1], v[34:35]
	v_pk_add_f32 v[2:3], v[2:3], v[36:37]
	v_pk_add_f32 v[0:1], v[0:1], v[30:31]
	v_pk_add_f32 v[2:3], v[2:3], v[32:33]
	v_pk_add_f32 v[0:1], v[0:1], v[26:27]
	v_pk_add_f32 v[2:3], v[2:3], v[28:29]
	v_pk_add_f32 v[0:1], v[0:1], v[22:23]
	v_pk_add_f32 v[2:3], v[2:3], v[24:25]
	v_pk_add_f32 v[0:1], v[0:1], v[18:19]
	v_pk_add_f32 v[2:3], v[2:3], v[20:21]
	v_pk_add_f32 v[0:1], v[0:1], v[10:11]
	v_pk_add_f32 v[2:3], v[2:3], v[12:13]
	v_pk_add_f32 v[0:1], v[0:1], v[6:7]
	v_pk_add_f32 v[2:3], v[2:3], v[8:9]
	s_mov_b64 s[24:25], exec
	s_mov_b32 exec_lo, 0
	s_brev_b32 exec_hi, 1
	v_mul_f32_e32 v52, -0.5, v52
	v_mul_f32_e32 v53, -0.5, v53
	v_mul_f32_e32 v54, -0.5, v54
	v_mul_f32_e32 v55, -0.5, v55
	v_mul_f32_e32 v56, -0.5, v56
	v_mul_f32_e32 v57, -0.5, v57
	v_mul_f32_e32 v58, -0.5, v58
	v_mul_f32_e32 v59, -0.5, v59
	v_cndmask_b32_e64 v52, v52, v66, s[16:17]
	v_cndmask_b32_e64 v53, v53, v66, s[14:15]
	v_cndmask_b32_e64 v54, v54, v66, s[12:13]
	v_cndmask_b32_e64 v55, v55, v66, s[10:11]
	v_cndmask_b32_e64 v56, v56, v66, s[8:9]
	v_cndmask_b32_e64 v57, v57, v66, s[6:7]
	v_cndmask_b32_e64 v58, v58, v66, s[4:5]
	v_cndmask_b32_e64 v59, v59, v66, s[2:3]
	v_lshlrev_b32_e32 v61, 2, v39
	global_store_dwordx4 v61, v[52:55], s[22:23]
	global_store_dwordx4 v61, v[56:59], s[22:23] offset:16
	s_mov_b64 exec, s[24:25]
	s_load_dwordx2 s[6:7], s[0:1], 0x18
	v_lshl_or_b32 v4, v44, 10, v40
	ds_write_b128 v4, v[0:3] offset:16384
	s_waitcnt lgkmcnt(0)
	s_barrier
	v_lshrrev_b32_e32 v12, 5, v38
	v_and_b32_e32 v12, 0x70, v12
	v_xor_b32_e32 v12, v38, v12
	ds_read_b128 v[0:3], v12
	ds_read_b128 v[4:7], v12 offset:4096
	v_mov_b32_e32 v39, 0
	v_lshl_add_u64 v[8:9], s[18:19], 0, v[38:39]
	s_movk_i32 s0, 0x2000
	s_waitcnt lgkmcnt(1)
	global_store_dwordx4 v38, v[0:3], s[18:19]
	ds_read_b128 v[0:3], v12 offset:8192
	v_add_co_u32_e32 v10, vcc, s0, v8
	s_movk_i32 s0, 0x3000
	s_nop 0
	v_addc_co_u32_e32 v11, vcc, 0, v9, vcc
	s_waitcnt lgkmcnt(1)
	global_store_dwordx4 v[10:11], v[4:7], off offset:-4096
	ds_read_b128 v[4:7], v12 offset:12288
	s_waitcnt lgkmcnt(1)
	global_store_dwordx4 v[10:11], v[0:3], off
	ds_read2st64_b32 v[0:1], v45 offset0:64 offset1:68
	ds_read2st64_b32 v[2:3], v45 offset0:72 offset1:76
	v_add_co_u32_e32 v8, vcc, s0, v8
	s_lshl_b64 s[0:1], s[20:21], 10
	s_waitcnt lgkmcnt(1)
	v_add_f32_e32 v0, v0, v1
	s_waitcnt lgkmcnt(0)
	v_add_f32_e32 v0, v0, v2
	s_add_u32 s0, s6, s0
	v_addc_co_u32_e32 v9, vcc, 0, v9, vcc
	v_add_f32_e32 v0, v0, v3
	s_addc_u32 s1, s7, s1
	global_store_dwordx4 v[8:9], v[4:7], off
	global_store_dword v45, v0, s[0:1]

.Lw1_e:
	v_add3_u32 v5, v108, v4, s2
	v_lshl_or_b32 v4, v118, 2, v4
	s_mov_b64 s[2:3], 0x14280
	s_waitcnt lgkmcnt(0)
	s_barrier
	v_add_u32_e32 v4, 0x18400, v4
	v_lshl_add_u64 v[2:3], v[2:3], 0, s[2:3]
	ds_read_b128 v[88:91], v5
	ds_read_b128 v[84:87], v5 offset:1024
	ds_read_b128 v[80:83], v5 offset:2048
	ds_read_b128 v[76:79], v5 offset:3072
	ds_read_b128 v[72:75], v5 offset:4096
	ds_read_b128 v[68:71], v5 offset:5120
	ds_read_b128 v[64:67], v5 offset:6144
	ds_read_b128 v[60:63], v5 offset:7168
	ds_read_b128 v[56:59], v5 offset:8192
	ds_read_b128 v[52:55], v5 offset:9216
	ds_read_b128 v[48:51], v5 offset:10240
	ds_read_b128 v[44:47], v5 offset:11264
	ds_read_b128 v[40:43], v5 offset:12288
	ds_read_b128 v[36:39], v5 offset:13312
	ds_read_b128 v[32:35], v5 offset:14336
	ds_read_b128 v[28:31], v5 offset:15360
	ds_read_b32 v116, v4
	s_waitcnt lgkmcnt(0)
	v_mul_f32_e32 v116, -2.0, v116
	v_lshl_add_u64 v[4:5], v[2:3], 0, v[6:7]
	v_add_u32_e32 v7, 0x14280, v6
	s_barrier
	v_readfirstlane_b32 s2, v7
	v_add_u32_e32 v7, 0x17280, v6
	s_mov_b32 m0, s2
	v_mov_b32_e32 v15, v109
	v_readfirstlane_b32 s2, v7
	v_add_u32_e32 v7, 0x1a280, v6
	global_load_lds_dwordx4 v[4:5], off
	v_lshl_add_u64 v[4:5], v[2:3], 0, v[14:15]
	s_mov_b32 m0, s2
	v_mov_b32_e32 v17, v109
	v_readfirstlane_b32 s2, v7
	v_add_u32_e32 v7, 0x1d280, v6
	global_load_lds_dwordx4 v[4:5], off
	v_lshl_add_u64 v[4:5], v[2:3], 0, v[16:17]
	s_mov_b32 m0, s2
	v_mov_b32_e32 v19, v109
	v_readfirstlane_b32 s2, v7
	global_load_lds_dwordx4 v[4:5], off
	v_lshl_add_u64 v[4:5], v[2:3], 0, v[18:19]
	s_mov_b32 m0, s2
	v_bfe_u32 v117, v0, 5, 1
	global_load_lds_dwordx4 v[4:5], off
	v_or_b32_e32 v4, 0xc000, v6
	v_add_u32_e32 v6, 0x20280, v6
	v_mov_b32_e32 v5, v109
	v_readfirstlane_b32 s2, v6
	v_lshl_add_u64 v[4:5], v[2:3], 0, v[4:5]
	s_mov_b32 m0, s2
	v_add_u32_e32 v131, 33, v115
	global_load_lds_dwordx4 v[4:5], off
	v_min_u32_e32 v4, 4, v27
	v_lshlrev_b32_e32 v6, 10, v4
	v_add_u32_e32 v4, 0xf000, v6
	v_mov_b32_e32 v5, v109
	v_lshl_add_u64 v[2:3], v[2:3], 0, v[4:5]
	v_add_u32_e32 v4, 0x23280, v6
	s_movk_i32 s73, 0x4080
	v_readfirstlane_b32 s2, v4
	s_mov_b32 m0, s2
	v_mov_b32_e32 v18, 0xff800000
	global_load_lds_dwordx4 v[2:3], off
	v_mul_u32_u24_e32 v2, 0x4080, v115
	v_lshl_or_b32 v2, v117, 4, v2
	v_add_u32_e32 v132, 0x4000, v2
	v_lshl_or_b32 v2, s59, 2, v119
	v_sub_u32_e32 v134, v2, v115
	v_add_u32_e32 v2, s72, v131
	v_ashrrev_i32_e32 v3, 31, v2
	v_lshlrev_b64 v[2:3], 10, v[2:3]
	v_lshl_or_b32 v2, v1, 2, v2
	v_lshl_add_u64 v[110:111], s[0:1], 0, v[108:109]
	v_cmp_gt_i32_e64 s[0:1], s78, v131
	v_mad_u32_u24 v133, v115, s73, v108
	v_lshl_add_u64 v[112:113], s[60:61], 0, v[2:3]
	s_mov_b64 s[60:61], -1
	v_mov_b32_e32 v135, 0x4080
	v_mov_b32_e32 v136, 0xff800000
	v_mov_b32_e32 v137, 0
	s_mov_b32 s81, s79
	v_mov_b32_e32 v1, v18
	v_mov_b32_e32 v20, v18
	v_mov_b32_e32 v19, v18
	v_mov_b32_e32 v24, v18
	v_mov_b32_e32 v23, v18
	v_mov_b32_e32 v22, v18
	v_mov_b32_e32 v21, v18
	v_mov_b32_e32 v26, v18
	v_mov_b32_e32 v25, v18
	s_and_b64 vcc, exec, s[68:69]
	s_cbranch_vccnz .Lw2_d
	s_waitcnt vmcnt(7)
	s_branch .Lw2_e

.LBB1_10:
	s_or_b64 exec, exec, s[74:75]
	s_nop 6
	v_mov_b32_e32 v107, v5
	v_med3_f32 v5, v26, v25, v2
	v_med3_f32 v25, v21, v26, v2
	v_med3_f32 v21, v22, v21, v2
	v_med3_f32 v22, v23, v22, v2
	v_med3_f32 v23, v24, v23, v2
	v_med3_f32 v24, v19, v24, v2
	v_med3_f32 v19, v20, v19, v2
	v_med3_f32 v20, v1, v20, v2
	v_med3_f32 v1, v18, v1, v2
	v_max_f32_e32 v18, v18, v18
	v_max_f32_e32 v2, v18, v2
	v_med3_f32 v5, v25, v5, v3
	v_med3_f32 v18, v21, v25, v3
	v_med3_f32 v21, v22, v21, v3
	v_med3_f32 v22, v23, v22, v3
	v_med3_f32 v23, v24, v23, v3
	v_med3_f32 v24, v19, v24, v3
	v_med3_f32 v19, v20, v19, v3
	v_med3_f32 v20, v1, v20, v3
	v_med3_f32 v1, v2, v1, v3
	v_max_f32_e32 v2, v2, v3
	v_med3_f32 v3, v18, v5, v4
	v_med3_f32 v5, v21, v18, v4
	v_med3_f32 v18, v22, v21, v4
	v_med3_f32 v21, v23, v22, v4
	v_med3_f32 v22, v24, v23, v4
	v_med3_f32 v23, v19, v24, v4
	v_med3_f32 v19, v20, v19, v4
	v_med3_f32 v20, v1, v20, v4
	v_med3_f32 v1, v2, v1, v4
	v_max_f32_e32 v2, v2, v4
	v_med3_f32 v3, v5, v3, v107
	v_med3_f32 v4, v18, v5, v107
	v_med3_f32 v5, v21, v18, v107
	v_med3_f32 v18, v22, v21, v107
	v_med3_f32 v21, v23, v22, v107
	v_med3_f32 v22, v19, v23, v107
	v_med3_f32 v19, v20, v19, v107
	v_med3_f32 v20, v1, v20, v107
	v_med3_f32 v1, v2, v1, v107
	v_max_f32_e32 v2, v2, v107
	v_mov_b32_e32 v103, v9
	v_med3_f32 v3, v4, v3, v6
	v_med3_f32 v4, v5, v4, v6
	v_med3_f32 v5, v18, v5, v6
	v_med3_f32 v9, v21, v18, v6
	v_med3_f32 v18, v22, v21, v6
	v_med3_f32 v21, v19, v22, v6
	v_med3_f32 v19, v20, v19, v6
	v_med3_f32 v20, v1, v20, v6
	v_med3_f32 v1, v2, v1, v6
	v_max_f32_e32 v2, v2, v6
	v_med3_f32 v3, v4, v3, v7
	v_med3_f32 v4, v5, v4, v7
	v_med3_f32 v5, v9, v5, v7
	v_med3_f32 v6, v18, v9, v7
	v_med3_f32 v9, v21, v18, v7
	v_med3_f32 v18, v19, v21, v7
	v_med3_f32 v19, v20, v19, v7
	v_med3_f32 v20, v1, v20, v7
	v_med3_f32 v1, v2, v1, v7
	v_max_f32_e32 v2, v2, v7
	v_med3_f32 v3, v4, v3, v8
	v_med3_f32 v4, v5, v4, v8
	v_med3_f32 v5, v6, v5, v8
	v_med3_f32 v6, v9, v6, v8
	v_med3_f32 v7, v18, v9, v8
	v_med3_f32 v9, v19, v18, v8
	v_med3_f32 v18, v20, v19, v8
	v_med3_f32 v19, v1, v20, v8
	v_med3_f32 v1, v2, v1, v8
	v_max_f32_e32 v2, v2, v8
	v_med3_f32 v3, v4, v3, v103
	v_med3_f32 v4, v5, v4, v103
	v_med3_f32 v5, v6, v5, v103
	v_med3_f32 v6, v7, v6, v103
	v_med3_f32 v7, v9, v7, v103
	v_med3_f32 v8, v18, v9, v103
	v_med3_f32 v9, v19, v18, v103
	v_med3_f32 v18, v1, v19, v103
	v_med3_f32 v1, v2, v1, v103
	v_max_f32_e32 v2, v2, v103
	v_mov_b32_e32 v99, v13
	v_med3_f32 v3, v4, v3, v10
	v_med3_f32 v4, v5, v4, v10
	v_med3_f32 v5, v6, v5, v10
	v_med3_f32 v6, v7, v6, v10
	v_med3_f32 v7, v8, v7, v10
	v_med3_f32 v8, v9, v8, v10
	v_med3_f32 v9, v18, v9, v10
	v_med3_f32 v13, v1, v18, v10
	v_med3_f32 v1, v2, v1, v10
	v_max_f32_e32 v2, v2, v10
	v_med3_f32 v3, v4, v3, v11
	v_med3_f32 v4, v5, v4, v11
	v_med3_f32 v5, v6, v5, v11
	v_med3_f32 v6, v7, v6, v11
	v_med3_f32 v7, v8, v7, v11
	v_med3_f32 v8, v9, v8, v11
	v_med3_f32 v9, v13, v9, v11
	v_med3_f32 v10, v1, v13, v11
	v_med3_f32 v1, v2, v1, v11
	v_max_f32_e32 v2, v2, v11
	v_med3_f32 v3, v4, v3, v12
	v_med3_f32 v4, v5, v4, v12
	v_med3_f32 v5, v6, v5, v12
	v_med3_f32 v6, v7, v6, v12
	v_med3_f32 v7, v8, v7, v12
	v_med3_f32 v8, v9, v8, v12
	v_med3_f32 v9, v10, v9, v12
	v_med3_f32 v10, v1, v10, v12
	v_med3_f32 v1, v2, v1, v12
	v_max_f32_e32 v2, v2, v12
	v_med3_f32 v3, v4, v3, v99
	v_med3_f32 v4, v5, v4, v99
	v_med3_f32 v5, v6, v5, v99
	v_med3_f32 v6, v7, v6, v99
	v_med3_f32 v7, v8, v7, v99
	v_med3_f32 v8, v9, v8, v99
	v_med3_f32 v9, v10, v9, v99
	v_med3_f32 v10, v1, v10, v99
	v_med3_f32 v1, v2, v1, v99
	v_max_f32_e32 v2, v2, v99
	v_mov_b32_e32 v11, v14
	v_mov_b32_e32 v12, v15
	v_med3_f32 v3, v4, v3, v11
	v_med3_f32 v4, v5, v4, v11
	v_med3_f32 v5, v6, v5, v11
	v_med3_f32 v6, v7, v6, v11
	v_med3_f32 v7, v8, v7, v11
	v_med3_f32 v8, v9, v8, v11
	v_med3_f32 v9, v10, v9, v11
	v_med3_f32 v10, v1, v10, v11
	v_med3_f32 v1, v2, v1, v11
	v_max_f32_e32 v2, v2, v11
	v_mov_b32_e32 v13, v16
	v_med3_f32 v3, v4, v3, v12
	v_med3_f32 v4, v5, v4, v12
	v_med3_f32 v5, v6, v5, v12
	v_med3_f32 v6, v7, v6, v12
	v_med3_f32 v7, v8, v7, v12
	v_med3_f32 v8, v9, v8, v12
	v_med3_f32 v9, v10, v9, v12
	v_med3_f32 v10, v1, v10, v12
	v_med3_f32 v1, v2, v1, v12
	v_max_f32_e32 v2, v2, v12
	v_mov_b32_e32 v95, v17
	v_med3_f32 v3, v4, v3, v13
	v_med3_f32 v4, v5, v4, v13
	v_med3_f32 v5, v6, v5, v13
	v_med3_f32 v6, v7, v6, v13
	v_med3_f32 v7, v8, v7, v13
	v_med3_f32 v8, v9, v8, v13
	v_med3_f32 v9, v10, v9, v13
	v_med3_f32 v10, v1, v10, v13
	v_med3_f32 v1, v2, v1, v13
	v_max_f32_e32 v2, v2, v13
	v_med3_f32 v25, v4, v3, v95
	v_med3_f32 v26, v5, v4, v95
	v_med3_f32 v21, v6, v5, v95
	v_med3_f32 v22, v7, v6, v95
	v_med3_f32 v23, v8, v7, v95
	v_med3_f32 v24, v9, v8, v95
	v_med3_f32 v19, v10, v9, v95
	v_med3_f32 v20, v1, v10, v95
	v_med3_f32 v1, v2, v1, v95
	v_max_f32_e32 v18, v2, v95

.LBB1_18:
	v_cmp_lt_u32_e32 vcc, v139, v108
	s_and_saveexec_b64 s[72:73], vcc
	s_cbranch_execz .LBB1_11
	v_add_u32_e32 v141, s82, v133
	v_add_u32_e32 v158, s82, v132
	ds_read_b128 v[2:5], v158
	ds_read_b128 v[6:9], v158 offset:32
	ds_read_b128 v[10:13], v158 offset:64
	ds_read_b128 v[14:17], v158 offset:96
	ds_read_b128 v[160:163], v141
	ds_read_b128 v[92:95], v141 offset:1024
	ds_read_b128 v[96:99], v141 offset:2048
	ds_read_b128 v[100:103], v141 offset:3072
	ds_read_b128 v[104:107], v141 offset:4096
	ds_read_b128 v[142:145], v141 offset:5120
	ds_read_b128 v[146:149], v141 offset:6144
	ds_read_b128 v[150:153], v141 offset:7168
	ds_read_b128 v[154:157], v141 offset:15360
	s_waitcnt lgkmcnt(8)
	v_mfma_f32_32x32x16_f16 v[2:17], v[160:163], v[88:91], v[2:17]
	s_waitcnt lgkmcnt(7)
	v_mfma_f32_32x32x16_f16 v[2:17], v[92:95], v[84:87], v[2:17]
	ds_read_b128 v[92:95], v141 offset:8192
	s_waitcnt lgkmcnt(7)
	v_mfma_f32_32x32x16_f16 v[2:17], v[96:99], v[80:83], v[2:17]
	ds_read_b128 v[96:99], v141 offset:9216
	s_waitcnt lgkmcnt(7)
	v_mfma_f32_32x32x16_f16 v[2:17], v[100:103], v[76:79], v[2:17]
	ds_read_b128 v[100:103], v141 offset:10240
	s_waitcnt lgkmcnt(7)
	v_mfma_f32_32x32x16_f16 v[2:17], v[104:107], v[72:75], v[2:17]
	ds_read_b128 v[104:107], v141 offset:11264
	s_waitcnt lgkmcnt(7)
	v_mfma_f32_32x32x16_f16 v[2:17], v[142:145], v[68:71], v[2:17]
	ds_read_b128 v[142:145], v141 offset:12288
	s_waitcnt lgkmcnt(7)
	v_mfma_f32_32x32x16_f16 v[2:17], v[146:149], v[64:67], v[2:17]
	ds_read_b128 v[146:149], v141 offset:13312
	s_waitcnt lgkmcnt(7)
	v_mfma_f32_32x32x16_f16 v[2:17], v[150:153], v[60:63], v[2:17]
	ds_read_b128 v[150:153], v141 offset:14336
	s_waitcnt lgkmcnt(6)
	v_mfma_f32_32x32x16_f16 v[2:17], v[92:95], v[56:59], v[2:17]
	s_waitcnt lgkmcnt(5)
	v_mfma_f32_32x32x16_f16 v[2:17], v[96:99], v[52:55], v[2:17]
	s_waitcnt lgkmcnt(4)
	v_mfma_f32_32x32x16_f16 v[2:17], v[100:103], v[48:51], v[2:17]
	s_waitcnt lgkmcnt(3)
	v_mfma_f32_32x32x16_f16 v[2:17], v[104:107], v[44:47], v[2:17]
	s_waitcnt lgkmcnt(2)
	v_mfma_f32_32x32x16_f16 v[2:17], v[142:145], v[40:43], v[2:17]
	s_waitcnt lgkmcnt(1)
	v_mfma_f32_32x32x16_f16 v[2:17], v[146:149], v[36:39], v[2:17]
	s_waitcnt lgkmcnt(0)
	v_mfma_f32_32x32x16_f16 v[2:17], v[150:153], v[32:35], v[2:17]
	v_mfma_f32_32x32x16_f16 v[2:17], v[154:157], v[28:31], v[2:17]
	s_nop 3
	v_cmp_eq_u32_e32 vcc, s81, v140
	s_and_saveexec_b64 s[74:75], vcc
	s_cbranch_execz .LBB1_10
	s_nop 7
	v_lshrrev_b32_e32 v142, 1, v0
	v_and_b32_e32 v143, 3, v0
	v_and_or_b32 v142, v142, 12, v143
	v_bfe_u32 v143, v0, 2, 1
	v_cmp_eq_u32_e32 vcc, v117, v143
	v_mov_b32_e32 v143, 0xff
	s_nop 1
	v_cndmask_b32_e32 v142, v143, v142, vcc
	v_cmp_eq_u32_e64 s[84:85], 0, v142
	v_cmp_eq_u32_e64 s[86:87], 1, v142
	v_cmp_eq_u32_e64 s[88:89], 2, v142
	v_cndmask_b32_e64 v2, v2, v136, s[84:85]
	v_cmp_eq_u32_e64 s[84:85], 3, v142
	v_cndmask_b32_e64 v3, v3, v136, s[86:87]
	v_cmp_eq_u32_e64 s[86:87], 4, v142
	v_cndmask_b32_e64 v4, v4, v136, s[88:89]
	v_cmp_eq_u32_e64 s[88:89], 5, v142
	v_cndmask_b32_e64 v5, v5, v136, s[84:85]
	v_cmp_eq_u32_e64 s[84:85], 6, v142
	v_cndmask_b32_e64 v6, v6, v136, s[86:87]
	v_cmp_eq_u32_e64 s[86:87], 7, v142
	v_cndmask_b32_e64 v7, v7, v136, s[88:89]
	v_cmp_eq_u32_e64 s[88:89], 8, v142
	v_cndmask_b32_e64 v8, v8, v136, s[84:85]
	v_cmp_eq_u32_e64 s[84:85], 9, v142
	v_cndmask_b32_e64 v9, v9, v136, s[86:87]
	v_cmp_eq_u32_e64 s[86:87], 10, v142
	v_cndmask_b32_e64 v10, v10, v136, s[88:89]
	v_cmp_eq_u32_e64 s[88:89], 11, v142
	v_cndmask_b32_e64 v11, v11, v136, s[84:85]
	v_cmp_eq_u32_e64 s[84:85], 12, v142
	v_cndmask_b32_e64 v12, v12, v136, s[86:87]
	v_cmp_eq_u32_e64 s[86:87], 13, v142
	v_cndmask_b32_e64 v13, v13, v136, s[88:89]
	v_cmp_eq_u32_e64 s[88:89], 14, v142
	v_cndmask_b32_e64 v14, v14, v136, s[84:85]
	v_cmp_eq_u32_e64 s[84:85], 15, v142
	v_cndmask_b32_e64 v15, v15, v136, s[86:87]
	v_cndmask_b32_e64 v16, v16, v136, s[88:89]
	v_cndmask_b32_e64 v17, v17, v136, s[84:85]
	s_branch .LBB1_10

.LBB1_26:
	v_mul_f32_e32 v1, -2.0, v1
	v_mul_f32_e32 v18, -2.0, v18
	v_mul_f32_e32 v19, -2.0, v19
	v_mul_f32_e32 v20, -2.0, v20
	v_mul_f32_e32 v21, -2.0, v21
	v_mul_f32_e32 v22, -2.0, v22
	v_mul_f32_e32 v23, -2.0, v23
	v_mul_f32_e32 v24, -2.0, v24
	v_mul_f32_e32 v25, -2.0, v25
	v_mul_f32_e32 v26, -2.0, v26
	s_and_b64 vcc, exec, s[68:69]
	s_cbranch_vccz .Lt_nw
	v_mov_b32_e32 v2, 0x24800
	v_lshl_add_u32 v2, v0, 2, v2
	ds_write_b32 v2, v137

	.amdhsa_kernel _Z6k3_knnPKiPKfPKDF16_PfS5_S5_
		.amdhsa_group_segment_fixed_size 153664
		.amdhsa_private_segment_fixed_size 0
		.amdhsa_kernarg_size 48
		.amdhsa_user_sgpr_count 2
		.amdhsa_user_sgpr_dispatch_ptr 0
		.amdhsa_user_sgpr_queue_ptr 0
		.amdhsa_user_sgpr_kernarg_segment_ptr 1
		.amdhsa_user_sgpr_dispatch_id 0
		.amdhsa_user_sgpr_kernarg_preload_length 0
		.amdhsa_user_sgpr_kernarg_preload_offset 0
		.amdhsa_user_sgpr_private_segment_size 0
		.amdhsa_uses_dynamic_stack 0
		.amdhsa_enable_private_segment 0
		.amdhsa_system_sgpr_workgroup_id_x 1
		.amdhsa_system_sgpr_workgroup_id_y 0
		.amdhsa_system_sgpr_workgroup_id_z 0
		.amdhsa_system_sgpr_workgroup_info 0
		.amdhsa_system_vgpr_workitem_id 0
		.amdhsa_next_free_vgpr 164
		.amdhsa_next_free_sgpr 96
		.amdhsa_accum_offset 164
		.amdhsa_reserve_vcc 1
		.amdhsa_float_round_mode_32 0
		.amdhsa_float_round_mode_16_64 0
		.amdhsa_float_denorm_mode_32 3
		.amdhsa_float_denorm_mode_16_64 3
		.amdhsa_dx10_clamp 1
		.amdhsa_ieee_mode 1
		.amdhsa_fp16_overflow 0
		.amdhsa_tg_split 0
		.amdhsa_exception_fp_ieee_invalid_op 0
		.amdhsa_exception_fp_denorm_src 0
		.amdhsa_exception_fp_ieee_div_zero 0
		.amdhsa_exception_fp_ieee_overflow 0
		.amdhsa_exception_fp_ieee_underflow 0
		.amdhsa_exception_fp_ieee_inexact 0
		.amdhsa_exception_int_div_zero 0
	.end_amdhsa_kernel

amdhsa.kernels:
  - .agpr_count:     0
    .args:
      - .actual_access:  read_only
        .address_space:  global
        .offset:         0
        .size:           8
        .value_kind:     global_buffer
      - .actual_access:  read_only
        .address_space:  global
        .offset:         8
        .size:           8
        .value_kind:     global_buffer
      - .actual_access:  write_only
        .address_space:  global
        .offset:         16
        .size:           8
        .value_kind:     global_buffer
      - .actual_access:  write_only
        .address_space:  global
        .offset:         24
        .size:           8
        .value_kind:     global_buffer
      - .actual_access:  write_only
        .address_space:  global
        .offset:         32
        .size:           8
        .value_kind:     global_buffer
      - .actual_access:  write_only
        .address_space:  global
        .offset:         40
        .size:           8
        .value_kind:     global_buffer
    .group_segment_fixed_size: 20704
    .kernarg_segment_align: 8
    .kernarg_segment_size: 48
    .language:       OpenCL C
    .language_version:
      - 2
      - 0
    .max_flat_workgroup_size: 256
    .name:           _Z7k1_prepPKfPKiPiPfPDF16_S4_
    .private_segment_fixed_size: 0
    .sgpr_count:     69
    .sgpr_spill_count: 0
    .symbol:         _Z7k1_prepPKfPKiPiPfPDF16_S4_.kd
    .uniform_work_group_size: 1
    .uses_dynamic_stack: false
    .vgpr_count:     70
    .vgpr_spill_count: 0
    .wavefront_size: 64
  - .agpr_count:     0
    .args:
      - .actual_access:  read_only
        .address_space:  global
        .offset:         0
        .size:           8
        .value_kind:     global_buffer
      - .actual_access:  read_only
        .address_space:  global
        .offset:         8
        .size:           8
        .value_kind:     global_buffer
      - .address_space:  global
        .offset:         16
        .size:           8
        .value_kind:     global_buffer
      - .actual_access:  write_only
        .address_space:  global
        .offset:         24
        .size:           8
        .value_kind:     global_buffer
      - .actual_access:  write_only
        .address_space:  global
        .offset:         32
        .size:           8
        .value_kind:     global_buffer
      - .actual_access:  write_only
        .address_space:  global
        .offset:         40
        .size:           8
        .value_kind:     global_buffer
    .group_segment_fixed_size: 153664
    .kernarg_segment_align: 8
    .kernarg_segment_size: 48
    .language:       OpenCL C
    .language_version:
      - 2
      - 0
    .max_flat_workgroup_size: 768
    .name:           _Z6k3_knnPKiPKfPKDF16_PfS5_S5_
    .private_segment_fixed_size: 0
    .sgpr_count:     92
    .sgpr_spill_count: 0
    .symbol:         _Z6k3_knnPKiPKfPKDF16_PfS5_S5_.kd
    .uniform_work_group_size: 1
    .uses_dynamic_stack: false
    .vgpr_count:     164
    .vgpr_spill_count: 0
    .wavefront_size: 64
  - .agpr_count:     0
    .args:
      - .actual_access:  read_only
        .address_space:  global
        .offset:         0
        .size:           8
        .value_kind:     global_buffer
      - .actual_access:  read_only
        .address_space:  global
        .offset:         8
        .size:           8
        .value_kind:     global_buffer
      - .actual_access:  read_only
        .address_space:  global
        .offset:         16
        .size:           8
        .value_kind:     global_buffer
      - .actual_access:  read_only
        .address_space:  global
        .offset:         24
        .size:           8
        .value_kind:     global_buffer
      - .actual_access:  read_only
        .address_space:  global
        .offset:         32
        .size:           8
        .value_kind:     global_buffer
      - .actual_access:  read_only
        .address_space:  global
        .offset:         40
        .size:           8
        .value_kind:     global_buffer
      - .actual_access:  read_only
        .address_space:  global
        .offset:         48
        .size:           8
        .value_kind:     global_buffer
      - .actual_access:  read_only
        .address_space:  global
        .offset:         56
        .size:           8
        .value_kind:     global_buffer
      - .address_space:  global
        .offset:         64
        .size:           8
        .value_kind:     global_buffer
    .group_segment_fixed_size: 30784
    .kernarg_segment_align: 8
    .kernarg_segment_size: 72
    .language:       OpenCL C
    .language_version:
      - 2
      - 0
    .max_flat_workgroup_size: 1024
    .name:           _Z9k3b_mergePKiPKfS2_S2_S2_S2_S2_S2_Pf
    .private_segment_fixed_size: 0
    .sgpr_count:     56
    .sgpr_spill_count: 0
    .symbol:         _Z9k3b_mergePKiPKfS2_S2_S2_S2_S2_S2_Pf.kd
    .uniform_work_group_size: 1
    .uses_dynamic_stack: false
    .vgpr_count:     70
    .vgpr_spill_count: 0
    .wavefront_size: 64
